# GEMM K-loop back-edge targets aligned to 64 bytes (padding never executed)
# speedup vs baseline: 1.0003x; 1.0003x over previous
;     __device__ __forceinline__ size_t a_off(const Unit& u, const Gemm& g) const { size_t o = (size_t)u.pm * BM * g.lda * 2; if (MODE == 1) o += (size_t)(u.pn >> 1) * 512 * 2; return o; }
;     __device__ __forceinline__ size_t b_off(const Unit& u, const Gemm& g) const { return (size_t)u.pn * BM * g.ldb * 2; }
; template <class Epi, class Sched, bool ALIGN_EPI = true, bool SP2 = true, class Side = NoSide>
; __device__ __forceinline__ void gemm_phase(LAS unsigned char* lds, const Gemm g, const Sched& S, const Epi& E, const Side side = Side()) {
;     ...
;     for (;;) {
;         const bool has_next = S.next(ui + 1, nxt);
;         const char* nA = has_next ? (const char*)g.A + S.a_off(nxt, g) : cA; const char* nB = has_next ? (const char*)g.Bt + S.b_off(nxt, g) : cB;
;     ...
; #pragma unroll
;         for (int a = 0; a < 2; ++a)
; #pragma unroll
;             for (int b = 0; b < 2; ++b)
; #pragma unroll
;                 for (int m = 0; m < 4; ++m)
; #pragma unroll
;                     for (int n = 0; n < 2; ++n) acc[a][b][m][n] = (f32x4){0.f, 0.f, 0.f, 0.f};
;         cur = nxt; cA = nA; cB = nB; ++ui;
.LBB0_159:
	s_ashr_i32 s25, s24, 31
	s_lshl_b64 s[26:27], s[24:25], 20
	s_add_u32 s26, s47, s26
	s_addc_u32 s27, s48, s27
	s_and_b64 s[28:29], s[8:9], exec
	s_cselect_b32 s11, s27, s35
	s_cselect_b32 s25, s26, s34
	s_ashr_i32 s23, s22, 31
	s_lshl_b64 s[28:29], s[22:23], 20
	s_add_u32 s28, s49, s28
	s_addc_u32 s29, s50, s29
	s_and_b64 s[36:37], s[8:9], exec
	s_cselect_b32 s23, s29, s39
	s_cselect_b32 s77, s28, s38
	s_cmp_lg_u32 s31, 0
	s_cselect_b64 s[36:37], -1, 0
	s_add_u32 s78, s38, 0x100
	v_mov_b32_e32 v2, 0
	s_addc_u32 s79, s39, 0
	v_lshl_add_u64 v[216:217], s[34:35], 0, v[208:209]
	v_lshl_add_u64 v[218:219], s[34:35], 0, v[210:211]
	s_mov_b32 s80, -2
	s_mov_b64 s[38:39], 0
	v_mov_b32_e32 v3, v2
	v_mov_b32_e32 v4, v2
	v_mov_b32_e32 v5, v2
	v_mov_b32_e32 v6, v2
	v_mov_b32_e32 v7, v2
	v_mov_b32_e32 v8, v2
	v_mov_b32_e32 v9, v2
	v_mov_b32_e32 v18, v2
	v_mov_b32_e32 v19, v2
	v_mov_b32_e32 v20, v2
	v_mov_b32_e32 v21, v2
	v_mov_b32_e32 v22, v2
	v_mov_b32_e32 v23, v2
	v_mov_b32_e32 v24, v2
	v_mov_b32_e32 v25, v2
	v_mov_b32_e32 v34, v2
	v_mov_b32_e32 v35, v2
	v_mov_b32_e32 v36, v2
	v_mov_b32_e32 v37, v2
	v_mov_b32_e32 v38, v2
	v_mov_b32_e32 v39, v2
	v_mov_b32_e32 v40, v2
	v_mov_b32_e32 v41, v2
	v_mov_b32_e32 v50, v2
	v_mov_b32_e32 v51, v2
	v_mov_b32_e32 v52, v2
	v_mov_b32_e32 v53, v2
	v_mov_b32_e32 v54, v2
	v_mov_b32_e32 v55, v2
	v_mov_b32_e32 v56, v2
	v_mov_b32_e32 v57, v2
	v_mov_b32_e32 v10, v2
	v_mov_b32_e32 v11, v2
	v_mov_b32_e32 v12, v2
	v_mov_b32_e32 v13, v2
	v_mov_b32_e32 v14, v2
	v_mov_b32_e32 v15, v2
	v_mov_b32_e32 v16, v2
	v_mov_b32_e32 v17, v2
	v_mov_b32_e32 v26, v2
	v_mov_b32_e32 v27, v2
	v_mov_b32_e32 v28, v2
	v_mov_b32_e32 v29, v2
	v_mov_b32_e32 v30, v2
	v_mov_b32_e32 v31, v2
	v_mov_b32_e32 v32, v2
	v_mov_b32_e32 v33, v2
	v_mov_b32_e32 v42, v2
	v_mov_b32_e32 v43, v2
	v_mov_b32_e32 v44, v2
	v_mov_b32_e32 v45, v2
	v_mov_b32_e32 v46, v2
	v_mov_b32_e32 v47, v2
	v_mov_b32_e32 v48, v2
	v_mov_b32_e32 v49, v2
	v_mov_b32_e32 v58, v2
	v_mov_b32_e32 v59, v2
	v_mov_b32_e32 v60, v2
	v_mov_b32_e32 v61, v2
	v_mov_b32_e32 v62, v2
	v_mov_b32_e32 v63, v2
	v_mov_b32_e32 v64, v2
	v_mov_b32_e32 v65, v2
	v_mov_b32_e32 v66, v2
	v_mov_b32_e32 v67, v2
	v_mov_b32_e32 v68, v2
	v_mov_b32_e32 v69, v2
	v_mov_b32_e32 v70, v2
	v_mov_b32_e32 v71, v2
	v_mov_b32_e32 v72, v2
	v_mov_b32_e32 v73, v2
	v_mov_b32_e32 v82, v2
	v_mov_b32_e32 v83, v2
	v_mov_b32_e32 v84, v2
	v_mov_b32_e32 v85, v2
	v_mov_b32_e32 v86, v2
	v_mov_b32_e32 v87, v2
	v_mov_b32_e32 v88, v2
	v_mov_b32_e32 v89, v2
	v_mov_b32_e32 v98, v2
	v_mov_b32_e32 v99, v2
	v_mov_b32_e32 v100, v2
	v_mov_b32_e32 v101, v2
	v_mov_b32_e32 v102, v2
	v_mov_b32_e32 v103, v2
	v_mov_b32_e32 v104, v2
	v_mov_b32_e32 v105, v2
	v_mov_b32_e32 v114, v2
	v_mov_b32_e32 v115, v2
	v_mov_b32_e32 v116, v2
	v_mov_b32_e32 v117, v2
	v_mov_b32_e32 v118, v2
	v_mov_b32_e32 v119, v2
	v_mov_b32_e32 v120, v2
	v_mov_b32_e32 v121, v2
	v_mov_b32_e32 v74, v2
	v_mov_b32_e32 v75, v2
	v_mov_b32_e32 v76, v2
	v_mov_b32_e32 v77, v2
	v_mov_b32_e32 v78, v2
	v_mov_b32_e32 v79, v2
	v_mov_b32_e32 v80, v2
	v_mov_b32_e32 v81, v2
	v_mov_b32_e32 v90, v2
	v_mov_b32_e32 v91, v2
	v_mov_b32_e32 v92, v2
	v_mov_b32_e32 v93, v2
	v_mov_b32_e32 v94, v2
	v_mov_b32_e32 v95, v2
	v_mov_b32_e32 v96, v2
	v_mov_b32_e32 v97, v2
	v_mov_b32_e32 v106, v2
	v_mov_b32_e32 v107, v2
	v_mov_b32_e32 v108, v2
	v_mov_b32_e32 v109, v2
	v_mov_b32_e32 v110, v2
	v_mov_b32_e32 v111, v2
	v_mov_b32_e32 v112, v2
	v_mov_b32_e32 v113, v2
	v_mov_b32_e32 v122, v2
	v_mov_b32_e32 v123, v2
	v_mov_b32_e32 v124, v2
	v_mov_b32_e32 v125, v2
	v_mov_b32_e32 v126, v2
	v_mov_b32_e32 v127, v2
	v_mov_b32_e32 v128, v2
	v_mov_b32_e32 v129, v2
	s_branch .LBB0_161
	.p2alignl 6, 3212836864

;     __device__ __forceinline__ size_t a_off(const Unit& u, const Gemm& g) const { size_t o = (size_t)u.pm * BM * g.lda * 2; if (MODE == 1) o += (size_t)(u.pn >> 1) * 512 * 2; return o; }
;     __device__ __forceinline__ size_t b_off(const Unit& u, const Gemm& g) const { return (size_t)u.pn * BM * g.ldb * 2; }
; template <class Epi, class Sched, bool ALIGN_EPI = true, bool SP2 = true, class Side = NoSide>
; __device__ __forceinline__ void gemm_phase(LAS unsigned char* lds, const Gemm g, const Sched& S, const Epi& E, const Side side = Side()) {
;     ...
;     for (;;) {
;         const bool has_next = S.next(ui + 1, nxt);
;         const char* nA = has_next ? (const char*)g.A + S.a_off(nxt, g) : cA; const char* nB = has_next ? (const char*)g.Bt + S.b_off(nxt, g) : cB;
;     ...
; #pragma unroll
;         for (int a = 0; a < 2; ++a)
; #pragma unroll
;             for (int b = 0; b < 2; ++b)
; #pragma unroll
;                 for (int m = 0; m < 4; ++m)
; #pragma unroll
;                     for (int n = 0; n < 2; ++n) acc[a][b][m][n] = (f32x4){0.f, 0.f, 0.f, 0.f};
;         cur = nxt; cA = nA; cB = nB; ++ui;
.LBB0_305:
	s_ashr_i32 s17, s16, 31
	s_lshl_b64 s[20:21], s[16:17], 18
	s_add_u32 s20, s35, s20
	s_addc_u32 s21, s36, s21
	s_and_b64 s[8:9], s[8:9], exec
	s_cselect_b32 s17, s21, s25
	s_cselect_b32 s53, s20, s24
	s_cmp_lg_u32 s26, 0
	s_cselect_b64 s[8:9], -1, 0
	s_add_u32 s54, s24, 0x100
	v_mov_b32_e32 v2, 0
	s_addc_u32 s55, s25, 0
	v_lshl_add_u64 v[212:213], s[22:23], 0, v[204:205]
	v_lshl_add_u64 v[214:215], s[22:23], 0, v[206:207]
	s_mov_b32 s56, -2
	s_mov_b64 s[24:25], 0
	v_mov_b32_e32 v3, v2
	v_mov_b32_e32 v4, v2
	v_mov_b32_e32 v5, v2
	v_mov_b32_e32 v6, v2
	v_mov_b32_e32 v7, v2
	v_mov_b32_e32 v8, v2
	v_mov_b32_e32 v9, v2
	v_mov_b32_e32 v14, v2
	v_mov_b32_e32 v15, v2
	v_mov_b32_e32 v16, v2
	v_mov_b32_e32 v17, v2
	v_mov_b32_e32 v22, v2
	v_mov_b32_e32 v23, v2
	v_mov_b32_e32 v24, v2
	v_mov_b32_e32 v25, v2
	v_mov_b32_e32 v30, v2
	v_mov_b32_e32 v31, v2
	v_mov_b32_e32 v32, v2
	v_mov_b32_e32 v33, v2
	v_mov_b32_e32 v38, v2
	v_mov_b32_e32 v39, v2
	v_mov_b32_e32 v40, v2
	v_mov_b32_e32 v41, v2
	v_mov_b32_e32 v46, v2
	v_mov_b32_e32 v47, v2
	v_mov_b32_e32 v48, v2
	v_mov_b32_e32 v49, v2
	v_mov_b32_e32 v54, v2
	v_mov_b32_e32 v55, v2
	v_mov_b32_e32 v56, v2
	v_mov_b32_e32 v57, v2
	v_mov_b32_e32 v10, v2
	v_mov_b32_e32 v11, v2
	v_mov_b32_e32 v12, v2
	v_mov_b32_e32 v13, v2
	v_mov_b32_e32 v18, v2
	v_mov_b32_e32 v19, v2
	v_mov_b32_e32 v20, v2
	v_mov_b32_e32 v21, v2
	v_mov_b32_e32 v26, v2
	v_mov_b32_e32 v27, v2
	v_mov_b32_e32 v28, v2
	v_mov_b32_e32 v29, v2
	v_mov_b32_e32 v34, v2
	v_mov_b32_e32 v35, v2
	v_mov_b32_e32 v36, v2
	v_mov_b32_e32 v37, v2
	v_mov_b32_e32 v42, v2
	v_mov_b32_e32 v43, v2
	v_mov_b32_e32 v44, v2
	v_mov_b32_e32 v45, v2
	v_mov_b32_e32 v50, v2
	v_mov_b32_e32 v51, v2
	v_mov_b32_e32 v52, v2
	v_mov_b32_e32 v53, v2
	v_mov_b32_e32 v58, v2
	v_mov_b32_e32 v59, v2
	v_mov_b32_e32 v60, v2
	v_mov_b32_e32 v61, v2
	v_mov_b32_e32 v62, v2
	v_mov_b32_e32 v63, v2
	v_mov_b32_e32 v64, v2
	v_mov_b32_e32 v65, v2
	v_mov_b32_e32 v66, v2
	v_mov_b32_e32 v67, v2
	v_mov_b32_e32 v68, v2
	v_mov_b32_e32 v69, v2
	v_mov_b32_e32 v70, v2
	v_mov_b32_e32 v71, v2
	v_mov_b32_e32 v72, v2
	v_mov_b32_e32 v73, v2
	v_mov_b32_e32 v74, v2
	v_mov_b32_e32 v75, v2
	v_mov_b32_e32 v76, v2
	v_mov_b32_e32 v77, v2
	v_mov_b32_e32 v78, v2
	v_mov_b32_e32 v79, v2
	v_mov_b32_e32 v80, v2
	v_mov_b32_e32 v81, v2
	v_mov_b32_e32 v82, v2
	v_mov_b32_e32 v83, v2
	v_mov_b32_e32 v84, v2
	v_mov_b32_e32 v85, v2
	v_mov_b32_e32 v90, v2
	v_mov_b32_e32 v91, v2
	v_mov_b32_e32 v92, v2
	v_mov_b32_e32 v93, v2
	v_mov_b32_e32 v98, v2
	v_mov_b32_e32 v99, v2
	v_mov_b32_e32 v100, v2
	v_mov_b32_e32 v101, v2
	v_mov_b32_e32 v106, v2
	v_mov_b32_e32 v107, v2
	v_mov_b32_e32 v108, v2
	v_mov_b32_e32 v109, v2
	v_mov_b32_e32 v86, v2
	v_mov_b32_e32 v87, v2
	v_mov_b32_e32 v88, v2
	v_mov_b32_e32 v89, v2
	v_mov_b32_e32 v94, v2
	v_mov_b32_e32 v95, v2
	v_mov_b32_e32 v96, v2
	v_mov_b32_e32 v97, v2
	v_mov_b32_e32 v102, v2
	v_mov_b32_e32 v103, v2
	v_mov_b32_e32 v104, v2
	v_mov_b32_e32 v105, v2
	v_mov_b32_e32 v110, v2
	v_mov_b32_e32 v111, v2
	v_mov_b32_e32 v112, v2
	v_mov_b32_e32 v113, v2
	v_mov_b32_e32 v114, v2
	v_mov_b32_e32 v115, v2
	v_mov_b32_e32 v116, v2
	v_mov_b32_e32 v117, v2
	v_mov_b32_e32 v118, v2
	v_mov_b32_e32 v119, v2
	v_mov_b32_e32 v120, v2
	v_mov_b32_e32 v121, v2
	v_mov_b32_e32 v122, v2
	v_mov_b32_e32 v123, v2
	v_mov_b32_e32 v124, v2
	v_mov_b32_e32 v125, v2
	v_mov_b32_e32 v126, v2
	v_mov_b32_e32 v127, v2
	v_mov_b32_e32 v128, v2
	v_mov_b32_e32 v129, v2
	s_branch .LBB0_307
	.p2alignl 6, 3212836864

;     __device__ __forceinline__ size_t a_off(const Unit& u, const Gemm& g) const { size_t o = (size_t)u.pm * BM * g.lda * 2; if (MODE == 1) o += (size_t)(u.pn >> 1) * 512 * 2; return o; }
;     __device__ __forceinline__ size_t b_off(const Unit& u, const Gemm& g) const { return (size_t)u.pn * BM * g.ldb * 2; }
; template <class Epi, class Sched, bool ALIGN_EPI = true, bool SP2 = true, class Side = NoSide>
; __device__ __forceinline__ void gemm_phase(LAS unsigned char* lds, const Gemm g, const Sched& S, const Epi& E, const Side side = Side()) {
;     ...
;     for (;;) {
;         const bool has_next = S.next(ui + 1, nxt);
;         const char* nA = has_next ? (const char*)g.A + S.a_off(nxt, g) : cA; const char* nB = has_next ? (const char*)g.Bt + S.b_off(nxt, g) : cB;
;     ...
; #pragma unroll
;         for (int a = 0; a < 2; ++a)
; #pragma unroll
;             for (int b = 0; b < 2; ++b)
; #pragma unroll
;                 for (int m = 0; m < 4; ++m)
; #pragma unroll
;                     for (int n = 0; n < 2; ++n) acc[a][b][m][n] = (f32x4){0.f, 0.f, 0.f, 0.f};
;         cur = nxt; cA = nA; cB = nB; ++ui;
.LBB0_995:
	s_ashr_i32 s25, s24, 31
	s_lshl_b64 s[26:27], s[24:25], 19
	s_add_u32 s26, s49, s26
	s_addc_u32 s27, s51, s27
	s_and_b64 s[28:29], s[6:7], exec
	s_cselect_b32 s25, s27, s35
	s_cselect_b32 s67, s26, s34
	s_ashr_i32 s23, s22, 31
	s_lshl_b64 s[28:29], s[22:23], 19
	s_add_u32 s28, s52, s28
	s_addc_u32 s29, s53, s29
	s_and_b64 s[40:41], s[6:7], exec
	s_cselect_b32 s23, s29, s39
	s_cselect_b32 s68, s28, s38
	s_cmp_lg_u32 s36, 0
	s_cselect_b64 s[36:37], -1, 0
	s_add_u32 s69, s38, 0x100
	v_mov_b32_e32 v2, 0
	s_addc_u32 s70, s39, 0
	v_lshl_add_u64 v[212:213], s[34:35], 0, v[204:205]
	v_lshl_add_u64 v[214:215], s[34:35], 0, v[206:207]
	s_mov_b32 s71, -2
	s_mov_b64 s[38:39], 0
	v_mov_b32_e32 v3, v2
	v_mov_b32_e32 v4, v2
	v_mov_b32_e32 v5, v2
	v_mov_b32_e32 v6, v2
	v_mov_b32_e32 v7, v2
	v_mov_b32_e32 v8, v2
	v_mov_b32_e32 v9, v2
	v_mov_b32_e32 v18, v2
	v_mov_b32_e32 v19, v2
	v_mov_b32_e32 v20, v2
	v_mov_b32_e32 v21, v2
	v_mov_b32_e32 v22, v2
	v_mov_b32_e32 v23, v2
	v_mov_b32_e32 v24, v2
	v_mov_b32_e32 v25, v2
	v_mov_b32_e32 v34, v2
	v_mov_b32_e32 v35, v2
	v_mov_b32_e32 v36, v2
	v_mov_b32_e32 v37, v2
	v_mov_b32_e32 v38, v2
	v_mov_b32_e32 v39, v2
	v_mov_b32_e32 v40, v2
	v_mov_b32_e32 v41, v2
	v_mov_b32_e32 v50, v2
	v_mov_b32_e32 v51, v2
	v_mov_b32_e32 v52, v2
	v_mov_b32_e32 v53, v2
	v_mov_b32_e32 v54, v2
	v_mov_b32_e32 v55, v2
	v_mov_b32_e32 v56, v2
	v_mov_b32_e32 v57, v2
	v_mov_b32_e32 v10, v2
	v_mov_b32_e32 v11, v2
	v_mov_b32_e32 v12, v2
	v_mov_b32_e32 v13, v2
	v_mov_b32_e32 v14, v2
	v_mov_b32_e32 v15, v2
	v_mov_b32_e32 v16, v2
	v_mov_b32_e32 v17, v2
	v_mov_b32_e32 v26, v2
	v_mov_b32_e32 v27, v2
	v_mov_b32_e32 v28, v2
	v_mov_b32_e32 v29, v2
	v_mov_b32_e32 v30, v2
	v_mov_b32_e32 v31, v2
	v_mov_b32_e32 v32, v2
	v_mov_b32_e32 v33, v2
	v_mov_b32_e32 v42, v2
	v_mov_b32_e32 v43, v2
	v_mov_b32_e32 v44, v2
	v_mov_b32_e32 v45, v2
	v_mov_b32_e32 v46, v2
	v_mov_b32_e32 v47, v2
	v_mov_b32_e32 v48, v2
	v_mov_b32_e32 v49, v2
	v_mov_b32_e32 v58, v2
	v_mov_b32_e32 v59, v2
	v_mov_b32_e32 v60, v2
	v_mov_b32_e32 v61, v2
	v_mov_b32_e32 v62, v2
	v_mov_b32_e32 v63, v2
	v_mov_b32_e32 v64, v2
	v_mov_b32_e32 v65, v2
	v_mov_b32_e32 v82, v2
	v_mov_b32_e32 v83, v2
	v_mov_b32_e32 v84, v2
	v_mov_b32_e32 v85, v2
	v_mov_b32_e32 v86, v2
	v_mov_b32_e32 v87, v2
	v_mov_b32_e32 v88, v2
	v_mov_b32_e32 v89, v2
	v_mov_b32_e32 v98, v2
	v_mov_b32_e32 v99, v2
	v_mov_b32_e32 v100, v2
	v_mov_b32_e32 v101, v2
	v_mov_b32_e32 v102, v2
	v_mov_b32_e32 v103, v2
	v_mov_b32_e32 v104, v2
	v_mov_b32_e32 v105, v2
	v_mov_b32_e32 v114, v2
	v_mov_b32_e32 v115, v2
	v_mov_b32_e32 v116, v2
	v_mov_b32_e32 v117, v2
	v_mov_b32_e32 v118, v2
	v_mov_b32_e32 v119, v2
	v_mov_b32_e32 v120, v2
	v_mov_b32_e32 v121, v2
	v_mov_b32_e32 v130, v2
	v_mov_b32_e32 v131, v2
	v_mov_b32_e32 v132, v2
	v_mov_b32_e32 v133, v2
	v_mov_b32_e32 v134, v2
	v_mov_b32_e32 v135, v2
	v_mov_b32_e32 v136, v2
	v_mov_b32_e32 v137, v2
	v_mov_b32_e32 v90, v2
	v_mov_b32_e32 v91, v2
	v_mov_b32_e32 v92, v2
	v_mov_b32_e32 v93, v2
	v_mov_b32_e32 v94, v2
	v_mov_b32_e32 v95, v2
	v_mov_b32_e32 v96, v2
	v_mov_b32_e32 v97, v2
	v_mov_b32_e32 v106, v2
	v_mov_b32_e32 v107, v2
	v_mov_b32_e32 v108, v2
	v_mov_b32_e32 v109, v2
	v_mov_b32_e32 v110, v2
	v_mov_b32_e32 v111, v2
	v_mov_b32_e32 v112, v2
	v_mov_b32_e32 v113, v2
	v_mov_b32_e32 v122, v2
	v_mov_b32_e32 v123, v2
	v_mov_b32_e32 v124, v2
	v_mov_b32_e32 v125, v2
	v_mov_b32_e32 v126, v2
	v_mov_b32_e32 v127, v2
	v_mov_b32_e32 v128, v2
	v_mov_b32_e32 v129, v2
	v_mov_b32_e32 v138, v2
	v_mov_b32_e32 v139, v2
	v_mov_b32_e32 v140, v2
	v_mov_b32_e32 v141, v2
	v_mov_b32_e32 v66, v2
	v_mov_b32_e32 v67, v2
	v_mov_b32_e32 v68, v2
	v_mov_b32_e32 v69, v2
	s_branch .LBB0_997
	.p2alignl 6, 3212836864

;     __device__ __forceinline__ size_t a_off(const Unit& u, const Gemm& g) const { size_t o = (size_t)u.pm * BM * g.lda * 2; if (MODE == 1) o += (size_t)(u.pn >> 1) * 512 * 2; return o; }
;     __device__ __forceinline__ size_t b_off(const Unit& u, const Gemm& g) const { return (size_t)u.pn * BM * g.ldb * 2; }
; template <class Epi, class Sched, bool ALIGN_EPI = true, bool SP2 = true, class Side = NoSide>
; __device__ __forceinline__ void gemm_phase(LAS unsigned char* lds, const Gemm g, const Sched& S, const Epi& E, const Side side = Side()) {
;     ...
;     for (;;) {
;         const bool has_next = S.next(ui + 1, nxt);
;         const char* nA = has_next ? (const char*)g.A + S.a_off(nxt, g) : cA; const char* nB = has_next ? (const char*)g.Bt + S.b_off(nxt, g) : cB;
;     ...
; #pragma unroll
;         for (int a = 0; a < 2; ++a)
; #pragma unroll
;             for (int b = 0; b < 2; ++b)
; #pragma unroll
;                 for (int m = 0; m < 4; ++m)
; #pragma unroll
;                     for (int n = 0; n < 2; ++n) acc[a][b][m][n] = (f32x4){0.f, 0.f, 0.f, 0.f};
;         cur = nxt; cA = nA; cB = nB; ++ui;
.LBB0_1022:
	s_ashr_i32 s27, s26, 31
	s_lshl_b64 s[28:29], s[26:27], 19
	s_add_u32 s28, s52, s28
	s_addc_u32 s29, s53, s29
	s_and_b64 s[30:31], s[8:9], exec
	s_cselect_b32 s27, s29, s39
	s_cselect_b32 s35, s28, s38
	s_ashr_i32 s25, s24, 31
	s_lshl_b64 s[30:31], s[24:25], 19
	s_add_u32 s30, s54, s30
	s_addc_u32 s31, s55, s31
	s_and_b64 s[44:45], s[8:9], exec
	s_cselect_b32 s25, s31, s43
	s_cselect_b32 s67, s30, s42
	s_cmp_lg_u32 s40, 0
	s_cselect_b64 s[40:41], -1, 0
	s_add_u32 s68, s42, 0x100
	v_mov_b32_e32 v2, 0
	s_addc_u32 s69, s43, 0
	v_lshl_add_u64 v[212:213], s[38:39], 0, v[204:205]
	v_lshl_add_u64 v[214:215], s[38:39], 0, v[206:207]
	s_mov_b32 s70, -2
	s_mov_b64 s[42:43], 0
	s_waitcnt lgkmcnt(0)
	v_mov_b32_e32 v3, v2
	v_mov_b32_e32 v4, v2
	v_mov_b32_e32 v5, v2
	v_mov_b32_e32 v6, v2
	v_mov_b32_e32 v7, v2
	v_mov_b32_e32 v8, v2
	v_mov_b32_e32 v9, v2
	v_mov_b32_e32 v18, v2
	v_mov_b32_e32 v19, v2
	v_mov_b32_e32 v20, v2
	v_mov_b32_e32 v21, v2
	v_mov_b32_e32 v22, v2
	v_mov_b32_e32 v23, v2
	v_mov_b32_e32 v24, v2
	v_mov_b32_e32 v25, v2
	v_mov_b32_e32 v34, v2
	v_mov_b32_e32 v35, v2
	v_mov_b32_e32 v36, v2
	v_mov_b32_e32 v37, v2
	v_mov_b32_e32 v38, v2
	v_mov_b32_e32 v39, v2
	v_mov_b32_e32 v40, v2
	v_mov_b32_e32 v41, v2
	v_mov_b32_e32 v58, v2
	v_mov_b32_e32 v59, v2
	v_mov_b32_e32 v60, v2
	v_mov_b32_e32 v61, v2
	v_mov_b32_e32 v70, v2
	v_mov_b32_e32 v71, v2
	v_mov_b32_e32 v72, v2
	v_mov_b32_e32 v73, v2
	v_mov_b32_e32 v10, v2
	v_mov_b32_e32 v11, v2
	v_mov_b32_e32 v12, v2
	v_mov_b32_e32 v13, v2
	v_mov_b32_e32 v14, v2
	v_mov_b32_e32 v15, v2
	v_mov_b32_e32 v16, v2
	v_mov_b32_e32 v17, v2
	v_mov_b32_e32 v26, v2
	v_mov_b32_e32 v27, v2
	v_mov_b32_e32 v28, v2
	v_mov_b32_e32 v29, v2
	v_mov_b32_e32 v30, v2
	v_mov_b32_e32 v31, v2
	v_mov_b32_e32 v32, v2
	v_mov_b32_e32 v33, v2
	v_mov_b32_e32 v42, v2
	v_mov_b32_e32 v43, v2
	v_mov_b32_e32 v44, v2
	v_mov_b32_e32 v45, v2
	v_mov_b32_e32 v46, v2
	v_mov_b32_e32 v47, v2
	v_mov_b32_e32 v48, v2
	v_mov_b32_e32 v49, v2
	v_mov_b32_e32 v74, v2
	v_mov_b32_e32 v75, v2
	v_mov_b32_e32 v76, v2
	v_mov_b32_e32 v77, v2
	v_mov_b32_e32 v78, v2
	v_mov_b32_e32 v79, v2
	v_mov_b32_e32 v80, v2
	v_mov_b32_e32 v81, v2
	v_mov_b32_e32 v82, v2
	v_mov_b32_e32 v83, v2
	v_mov_b32_e32 v84, v2
	v_mov_b32_e32 v85, v2
	v_mov_b32_e32 v86, v2
	v_mov_b32_e32 v87, v2
	v_mov_b32_e32 v88, v2
	v_mov_b32_e32 v89, v2
	v_mov_b32_e32 v98, v2
	v_mov_b32_e32 v99, v2
	v_mov_b32_e32 v100, v2
	v_mov_b32_e32 v101, v2
	v_mov_b32_e32 v102, v2
	v_mov_b32_e32 v103, v2
	v_mov_b32_e32 v104, v2
	v_mov_b32_e32 v105, v2
	v_mov_b32_e32 v114, v2
	v_mov_b32_e32 v115, v2
	v_mov_b32_e32 v116, v2
	v_mov_b32_e32 v117, v2
	v_mov_b32_e32 v118, v2
	v_mov_b32_e32 v119, v2
	v_mov_b32_e32 v120, v2
	v_mov_b32_e32 v121, v2
	v_mov_b32_e32 v130, v2
	v_mov_b32_e32 v131, v2
	v_mov_b32_e32 v132, v2
	v_mov_b32_e32 v133, v2
	v_mov_b32_e32 v134, v2
	v_mov_b32_e32 v135, v2
	v_mov_b32_e32 v136, v2
	v_mov_b32_e32 v137, v2
	v_mov_b32_e32 v90, v2
	v_mov_b32_e32 v91, v2
	v_mov_b32_e32 v92, v2
	v_mov_b32_e32 v93, v2
	v_mov_b32_e32 v94, v2
	v_mov_b32_e32 v95, v2
	v_mov_b32_e32 v96, v2
	v_mov_b32_e32 v97, v2
	v_mov_b32_e32 v106, v2
	v_mov_b32_e32 v107, v2
	v_mov_b32_e32 v108, v2
	v_mov_b32_e32 v109, v2
	v_mov_b32_e32 v110, v2
	v_mov_b32_e32 v111, v2
	v_mov_b32_e32 v112, v2
	v_mov_b32_e32 v113, v2
	v_mov_b32_e32 v122, v2
	v_mov_b32_e32 v123, v2
	v_mov_b32_e32 v124, v2
	v_mov_b32_e32 v125, v2
	v_mov_b32_e32 v126, v2
	v_mov_b32_e32 v127, v2
	v_mov_b32_e32 v128, v2
	v_mov_b32_e32 v129, v2
	v_mov_b32_e32 v50, v2
	v_mov_b32_e32 v51, v2
	v_mov_b32_e32 v52, v2
	v_mov_b32_e32 v53, v2
	v_mov_b32_e32 v54, v2
	v_mov_b32_e32 v55, v2
	v_mov_b32_e32 v56, v2
	v_mov_b32_e32 v57, v2
	s_branch .LBB0_1024
	.p2alignl 6, 3212836864

;     __device__ __forceinline__ size_t a_off(const Unit& u, const Gemm& g) const { size_t o = (size_t)u.pm * BM * g.lda * 2; if (MODE == 1) o += (size_t)(u.pn >> 1) * 512 * 2; return o; }
;     __device__ __forceinline__ size_t b_off(const Unit& u, const Gemm& g) const { return (size_t)u.pn * BM * g.ldb * 2; }
; template <class Epi, class Sched, bool ALIGN_EPI = true, bool SP2 = true, class Side = NoSide>
; __device__ __forceinline__ void gemm_phase(LAS unsigned char* lds, const Gemm g, const Sched& S, const Epi& E, const Side side = Side()) {
;     ...
;     for (;;) {
;         const bool has_next = S.next(ui + 1, nxt);
;         const char* nA = has_next ? (const char*)g.A + S.a_off(nxt, g) : cA; const char* nB = has_next ? (const char*)g.Bt + S.b_off(nxt, g) : cB;
;     ...
; #pragma unroll
;         for (int a = 0; a < 2; ++a)
; #pragma unroll
;             for (int b = 0; b < 2; ++b)
; #pragma unroll
;                 for (int m = 0; m < 4; ++m)
; #pragma unroll
;                     for (int n = 0; n < 2; ++n) acc[a][b][m][n] = (f32x4){0.f, 0.f, 0.f, 0.f};
;         cur = nxt; cA = nA; cB = nB; ++ui;
.LBB0_1180:
	s_ashr_i32 s21, s20, 31
	s_lshl_b64 s[22:23], s[20:21], 20
	s_add_u32 s22, s33, s22
	s_addc_u32 s23, s42, s23
	s_and_b64 s[24:25], s[6:7], exec
	s_cselect_b32 s21, s23, s29
	s_cselect_b32 s59, s22, s28
	s_ashr_i32 s17, s16, 31
	s_lshl_b64 s[24:25], s[16:17], 20
	s_add_u32 s24, s43, s24
	s_addc_u32 s25, s44, s25
	s_and_b64 s[36:37], s[6:7], exec
	s_cselect_b32 s17, s25, s35
	s_cselect_b32 s60, s24, s34
	s_cmp_lg_u32 s30, 0
	s_cselect_b64 s[30:31], -1, 0
	s_add_u32 s61, s34, 0x100
	v_mov_b32_e32 v2, 0
	s_addc_u32 s62, s35, 0
	v_lshl_add_u64 v[212:213], s[28:29], 0, v[204:205]
	v_lshl_add_u64 v[214:215], s[28:29], 0, v[206:207]
	s_mov_b32 s63, -2
	s_mov_b64 s[34:35], 0
	v_mov_b32_e32 v3, v2
	v_mov_b32_e32 v4, v2
	v_mov_b32_e32 v5, v2
	v_mov_b32_e32 v6, v2
	v_mov_b32_e32 v7, v2
	v_mov_b32_e32 v8, v2
	v_mov_b32_e32 v9, v2
	v_mov_b32_e32 v18, v2
	v_mov_b32_e32 v19, v2
	v_mov_b32_e32 v20, v2
	v_mov_b32_e32 v21, v2
	v_mov_b32_e32 v22, v2
	v_mov_b32_e32 v23, v2
	v_mov_b32_e32 v24, v2
	v_mov_b32_e32 v25, v2
	v_mov_b32_e32 v34, v2
	v_mov_b32_e32 v35, v2
	v_mov_b32_e32 v36, v2
	v_mov_b32_e32 v37, v2
	v_mov_b32_e32 v38, v2
	v_mov_b32_e32 v39, v2
	v_mov_b32_e32 v40, v2
	v_mov_b32_e32 v41, v2
	v_mov_b32_e32 v50, v2
	v_mov_b32_e32 v51, v2
	v_mov_b32_e32 v52, v2
	v_mov_b32_e32 v53, v2
	v_mov_b32_e32 v54, v2
	v_mov_b32_e32 v55, v2
	v_mov_b32_e32 v56, v2
	v_mov_b32_e32 v57, v2
	v_mov_b32_e32 v10, v2
	v_mov_b32_e32 v11, v2
	v_mov_b32_e32 v12, v2
	v_mov_b32_e32 v13, v2
	v_mov_b32_e32 v14, v2
	v_mov_b32_e32 v15, v2
	v_mov_b32_e32 v16, v2
	v_mov_b32_e32 v17, v2
	v_mov_b32_e32 v26, v2
	v_mov_b32_e32 v27, v2
	v_mov_b32_e32 v28, v2
	v_mov_b32_e32 v29, v2
	v_mov_b32_e32 v30, v2
	v_mov_b32_e32 v31, v2
	v_mov_b32_e32 v32, v2
	v_mov_b32_e32 v33, v2
	v_mov_b32_e32 v42, v2
	v_mov_b32_e32 v43, v2
	v_mov_b32_e32 v44, v2
	v_mov_b32_e32 v45, v2
	v_mov_b32_e32 v46, v2
	v_mov_b32_e32 v47, v2
	v_mov_b32_e32 v48, v2
	v_mov_b32_e32 v49, v2
	v_mov_b32_e32 v58, v2
	v_mov_b32_e32 v59, v2
	v_mov_b32_e32 v60, v2
	v_mov_b32_e32 v61, v2
	v_mov_b32_e32 v62, v2
	v_mov_b32_e32 v63, v2
	v_mov_b32_e32 v64, v2
	v_mov_b32_e32 v65, v2
	v_mov_b32_e32 v66, v2
	v_mov_b32_e32 v67, v2
	v_mov_b32_e32 v68, v2
	v_mov_b32_e32 v69, v2
	v_mov_b32_e32 v70, v2
	v_mov_b32_e32 v71, v2
	v_mov_b32_e32 v72, v2
	v_mov_b32_e32 v73, v2
	v_mov_b32_e32 v82, v2
	v_mov_b32_e32 v83, v2
	v_mov_b32_e32 v84, v2
	v_mov_b32_e32 v85, v2
	v_mov_b32_e32 v86, v2
	v_mov_b32_e32 v87, v2
	v_mov_b32_e32 v88, v2
	v_mov_b32_e32 v89, v2
	v_mov_b32_e32 v98, v2
	v_mov_b32_e32 v99, v2
	v_mov_b32_e32 v100, v2
	v_mov_b32_e32 v101, v2
	v_mov_b32_e32 v102, v2
	v_mov_b32_e32 v103, v2
	v_mov_b32_e32 v104, v2
	v_mov_b32_e32 v105, v2
	v_mov_b32_e32 v130, v2
	v_mov_b32_e32 v131, v2
	v_mov_b32_e32 v132, v2
	v_mov_b32_e32 v133, v2
	v_mov_b32_e32 v134, v2
	v_mov_b32_e32 v135, v2
	v_mov_b32_e32 v136, v2
	v_mov_b32_e32 v137, v2
	v_mov_b32_e32 v74, v2
	v_mov_b32_e32 v75, v2
	v_mov_b32_e32 v76, v2
	v_mov_b32_e32 v77, v2
	v_mov_b32_e32 v78, v2
	v_mov_b32_e32 v79, v2
	v_mov_b32_e32 v80, v2
	v_mov_b32_e32 v81, v2
	v_mov_b32_e32 v90, v2
	v_mov_b32_e32 v91, v2
	v_mov_b32_e32 v92, v2
	v_mov_b32_e32 v93, v2
	v_mov_b32_e32 v94, v2
	v_mov_b32_e32 v95, v2
	v_mov_b32_e32 v96, v2
	v_mov_b32_e32 v97, v2
	v_mov_b32_e32 v114, v2
	v_mov_b32_e32 v115, v2
	v_mov_b32_e32 v116, v2
	v_mov_b32_e32 v117, v2
	v_mov_b32_e32 v118, v2
	v_mov_b32_e32 v119, v2
	v_mov_b32_e32 v120, v2
	v_mov_b32_e32 v121, v2
	v_mov_b32_e32 v138, v2
	v_mov_b32_e32 v139, v2
	v_mov_b32_e32 v140, v2
	v_mov_b32_e32 v141, v2
	v_mov_b32_e32 v142, v2
	v_mov_b32_e32 v143, v2
	v_mov_b32_e32 v144, v2
	v_mov_b32_e32 v145, v2
	s_branch .LBB0_1182
	.p2alignl 6, 3212836864

;     __device__ __forceinline__ size_t a_off(const Unit& u, const Gemm& g) const { size_t o = (size_t)u.pm * BM * g.lda * 2; if (MODE == 1) o += (size_t)(u.pn >> 1) * 512 * 2; return o; }
;     __device__ __forceinline__ size_t b_off(const Unit& u, const Gemm& g) const { return (size_t)u.pn * BM * g.ldb * 2; }
; template <class Epi, class Sched, bool ALIGN_EPI = true, bool SP2 = true, class Side = NoSide>
; __device__ __forceinline__ void gemm_phase(LAS unsigned char* lds, const Gemm g, const Sched& S, const Epi& E, const Side side = Side()) {
;     ...
;     for (;;) {
;         const bool has_next = S.next(ui + 1, nxt);
;         const char* nA = has_next ? (const char*)g.A + S.a_off(nxt, g) : cA; const char* nB = has_next ? (const char*)g.Bt + S.b_off(nxt, g) : cB;
;     ...
; #pragma unroll
;         for (int a = 0; a < 2; ++a)
; #pragma unroll
;             for (int b = 0; b < 2; ++b)
; #pragma unroll
;                 for (int m = 0; m < 4; ++m)
; #pragma unroll
;                     for (int n = 0; n < 2; ++n) acc[a][b][m][n] = (f32x4){0.f, 0.f, 0.f, 0.f};
;         cur = nxt; cA = nA; cB = nB; ++ui;
.LBB0_1324:
	s_ashr_i32 s21, s20, 31
	s_lshl_b64 s[22:23], s[20:21], 20
	s_add_u32 s22, s33, s22
	s_addc_u32 s23, s42, s23
	s_and_b64 s[24:25], s[6:7], exec
	s_cselect_b32 s21, s23, s29
	s_cselect_b32 s60, s22, s28
	s_ashr_i32 s17, s16, 31
	s_lshl_b64 s[24:25], s[16:17], 20
	s_add_u32 s24, s43, s24
	s_addc_u32 s25, s44, s25
	s_and_b64 s[36:37], s[6:7], exec
	s_cselect_b32 s17, s25, s35
	s_cselect_b32 s61, s24, s34
	s_cmp_lg_u32 s30, 0
	s_cselect_b64 s[30:31], -1, 0
	s_add_u32 s62, s34, 0x100
	v_mov_b32_e32 v2, 0
	s_addc_u32 s63, s35, 0
	v_lshl_add_u64 v[212:213], s[28:29], 0, v[204:205]
	v_lshl_add_u64 v[214:215], s[28:29], 0, v[206:207]
	s_mov_b32 s64, -2
	s_mov_b64 s[34:35], 0
	v_mov_b32_e32 v3, v2
	v_mov_b32_e32 v4, v2
	v_mov_b32_e32 v5, v2
	v_mov_b32_e32 v6, v2
	v_mov_b32_e32 v7, v2
	v_mov_b32_e32 v8, v2
	v_mov_b32_e32 v9, v2
	v_mov_b32_e32 v18, v2
	v_mov_b32_e32 v19, v2
	v_mov_b32_e32 v20, v2
	v_mov_b32_e32 v21, v2
	v_mov_b32_e32 v22, v2
	v_mov_b32_e32 v23, v2
	v_mov_b32_e32 v24, v2
	v_mov_b32_e32 v25, v2
	v_mov_b32_e32 v34, v2
	v_mov_b32_e32 v35, v2
	v_mov_b32_e32 v36, v2
	v_mov_b32_e32 v37, v2
	v_mov_b32_e32 v38, v2
	v_mov_b32_e32 v39, v2
	v_mov_b32_e32 v40, v2
	v_mov_b32_e32 v41, v2
	v_mov_b32_e32 v50, v2
	v_mov_b32_e32 v51, v2
	v_mov_b32_e32 v52, v2
	v_mov_b32_e32 v53, v2
	v_mov_b32_e32 v54, v2
	v_mov_b32_e32 v55, v2
	v_mov_b32_e32 v56, v2
	v_mov_b32_e32 v57, v2
	v_mov_b32_e32 v10, v2
	v_mov_b32_e32 v11, v2
	v_mov_b32_e32 v12, v2
	v_mov_b32_e32 v13, v2
	v_mov_b32_e32 v14, v2
	v_mov_b32_e32 v15, v2
	v_mov_b32_e32 v16, v2
	v_mov_b32_e32 v17, v2
	v_mov_b32_e32 v26, v2
	v_mov_b32_e32 v27, v2
	v_mov_b32_e32 v28, v2
	v_mov_b32_e32 v29, v2
	v_mov_b32_e32 v30, v2
	v_mov_b32_e32 v31, v2
	v_mov_b32_e32 v32, v2
	v_mov_b32_e32 v33, v2
	v_mov_b32_e32 v42, v2
	v_mov_b32_e32 v43, v2
	v_mov_b32_e32 v44, v2
	v_mov_b32_e32 v45, v2
	v_mov_b32_e32 v46, v2
	v_mov_b32_e32 v47, v2
	v_mov_b32_e32 v48, v2
	v_mov_b32_e32 v49, v2
	v_mov_b32_e32 v58, v2
	v_mov_b32_e32 v59, v2
	v_mov_b32_e32 v60, v2
	v_mov_b32_e32 v61, v2
	v_mov_b32_e32 v62, v2
	v_mov_b32_e32 v63, v2
	v_mov_b32_e32 v64, v2
	v_mov_b32_e32 v65, v2
	v_mov_b32_e32 v66, v2
	v_mov_b32_e32 v67, v2
	v_mov_b32_e32 v68, v2
	v_mov_b32_e32 v69, v2
	v_mov_b32_e32 v70, v2
	v_mov_b32_e32 v71, v2
	v_mov_b32_e32 v72, v2
	v_mov_b32_e32 v73, v2
	v_mov_b32_e32 v82, v2
	v_mov_b32_e32 v83, v2
	v_mov_b32_e32 v84, v2
	v_mov_b32_e32 v85, v2
	v_mov_b32_e32 v86, v2
	v_mov_b32_e32 v87, v2
	v_mov_b32_e32 v88, v2
	v_mov_b32_e32 v89, v2
	v_mov_b32_e32 v98, v2
	v_mov_b32_e32 v99, v2
	v_mov_b32_e32 v100, v2
	v_mov_b32_e32 v101, v2
	v_mov_b32_e32 v102, v2
	v_mov_b32_e32 v103, v2
	v_mov_b32_e32 v104, v2
	v_mov_b32_e32 v105, v2
	v_mov_b32_e32 v118, v2
	v_mov_b32_e32 v119, v2
	v_mov_b32_e32 v120, v2
	v_mov_b32_e32 v121, v2
	v_mov_b32_e32 v126, v2
	v_mov_b32_e32 v127, v2
	v_mov_b32_e32 v128, v2
	v_mov_b32_e32 v129, v2
	v_mov_b32_e32 v74, v2
	v_mov_b32_e32 v75, v2
	v_mov_b32_e32 v76, v2
	v_mov_b32_e32 v77, v2
	v_mov_b32_e32 v78, v2
	v_mov_b32_e32 v79, v2
	v_mov_b32_e32 v80, v2
	v_mov_b32_e32 v81, v2
	v_mov_b32_e32 v90, v2
	v_mov_b32_e32 v91, v2
	v_mov_b32_e32 v92, v2
	v_mov_b32_e32 v93, v2
	v_mov_b32_e32 v94, v2
	v_mov_b32_e32 v95, v2
	v_mov_b32_e32 v96, v2
	v_mov_b32_e32 v97, v2
	v_mov_b32_e32 v106, v2
	v_mov_b32_e32 v107, v2
	v_mov_b32_e32 v108, v2
	v_mov_b32_e32 v109, v2
	v_mov_b32_e32 v110, v2
	v_mov_b32_e32 v111, v2
	v_mov_b32_e32 v112, v2
	v_mov_b32_e32 v113, v2
	v_mov_b32_e32 v138, v2
	v_mov_b32_e32 v139, v2
	v_mov_b32_e32 v140, v2
	v_mov_b32_e32 v141, v2
	v_mov_b32_e32 v142, v2
	v_mov_b32_e32 v143, v2
	v_mov_b32_e32 v144, v2
	v_mov_b32_e32 v145, v2
	s_branch .LBB0_1326
	.p2alignl 6, 3212836864

;     __device__ __forceinline__ size_t a_off(const Unit& u, const Gemm& g) const { size_t o = (size_t)u.pm * BM * g.lda * 2; if (MODE == 1) o += (size_t)(u.pn >> 1) * 512 * 2; return o; }
;     __device__ __forceinline__ size_t b_off(const Unit& u, const Gemm& g) const { return (size_t)u.pn * BM * g.ldb * 2; }
; template <class Epi, class Sched, bool ALIGN_EPI = true, bool SP2 = true, class Side = NoSide>
; __device__ __forceinline__ void gemm_phase(LAS unsigned char* lds, const Gemm g, const Sched& S, const Epi& E, const Side side = Side()) {
;     ...
;     for (;;) {
;         const bool has_next = S.next(ui + 1, nxt);
;         const char* nA = has_next ? (const char*)g.A + S.a_off(nxt, g) : cA; const char* nB = has_next ? (const char*)g.Bt + S.b_off(nxt, g) : cB;
;     ...
; #pragma unroll
;         for (int a = 0; a < 2; ++a)
; #pragma unroll
;             for (int b = 0; b < 2; ++b)
; #pragma unroll
;                 for (int m = 0; m < 4; ++m)
; #pragma unroll
;                     for (int n = 0; n < 2; ++n) acc[a][b][m][n] = (f32x4){0.f, 0.f, 0.f, 0.f};
;         cur = nxt; cA = nA; cB = nB; ++ui;
.LBB0_1729:
	s_ashr_i32 s23, s22, 31
	s_lshl_b64 s[24:25], s[22:23], 20
	s_add_u32 s24, s45, s24
	s_addc_u32 s25, s46, s25
	s_and_b64 s[26:27], s[6:7], exec
	s_cselect_b32 s23, s25, s31
	s_cselect_b32 s61, s24, s30
	s_ashr_i32 s21, s20, 31
	s_lshl_b64 s[26:27], s[20:21], 20
	s_add_u32 s26, s33, s26
	s_addc_u32 s27, s44, s27
	s_and_b64 s[38:39], s[6:7], exec
	s_cselect_b32 s21, s27, s37
	s_cselect_b32 s62, s26, s36
	s_cmp_lg_u32 s34, 0
	s_cselect_b64 s[34:35], -1, 0
	s_add_u32 s63, s36, 0x100
	v_mov_b32_e32 v0, 0
	s_addc_u32 s64, s37, 0
	v_lshl_add_u64 v[210:211], s[30:31], 0, v[202:203]
	v_lshl_add_u64 v[212:213], s[30:31], 0, v[204:205]
	s_mov_b32 s65, -2
	s_mov_b64 s[36:37], 0
	v_mov_b32_e32 v1, v0
	v_mov_b32_e32 v2, v0
	v_mov_b32_e32 v3, v0
	v_mov_b32_e32 v4, v0
	v_mov_b32_e32 v5, v0
	v_mov_b32_e32 v6, v0
	v_mov_b32_e32 v7, v0
	v_mov_b32_e32 v16, v0
	v_mov_b32_e32 v17, v0
	v_mov_b32_e32 v18, v0
	v_mov_b32_e32 v19, v0
	v_mov_b32_e32 v20, v0
	v_mov_b32_e32 v21, v0
	v_mov_b32_e32 v22, v0
	v_mov_b32_e32 v23, v0
	v_mov_b32_e32 v32, v0
	v_mov_b32_e32 v33, v0
	v_mov_b32_e32 v34, v0
	v_mov_b32_e32 v35, v0
	v_mov_b32_e32 v36, v0
	v_mov_b32_e32 v37, v0
	v_mov_b32_e32 v38, v0
	v_mov_b32_e32 v39, v0
	v_mov_b32_e32 v48, v0
	v_mov_b32_e32 v49, v0
	v_mov_b32_e32 v50, v0
	v_mov_b32_e32 v51, v0
	v_mov_b32_e32 v52, v0
	v_mov_b32_e32 v53, v0
	v_mov_b32_e32 v54, v0
	v_mov_b32_e32 v55, v0
	v_mov_b32_e32 v8, v0
	v_mov_b32_e32 v9, v0
	v_mov_b32_e32 v10, v0
	v_mov_b32_e32 v11, v0
	v_mov_b32_e32 v12, v0
	v_mov_b32_e32 v13, v0
	v_mov_b32_e32 v14, v0
	v_mov_b32_e32 v15, v0
	v_mov_b32_e32 v24, v0
	v_mov_b32_e32 v25, v0
	v_mov_b32_e32 v26, v0
	v_mov_b32_e32 v27, v0
	v_mov_b32_e32 v28, v0
	v_mov_b32_e32 v29, v0
	v_mov_b32_e32 v30, v0
	v_mov_b32_e32 v31, v0
	v_mov_b32_e32 v40, v0
	v_mov_b32_e32 v41, v0
	v_mov_b32_e32 v42, v0
	v_mov_b32_e32 v43, v0
	v_mov_b32_e32 v44, v0
	v_mov_b32_e32 v45, v0
	v_mov_b32_e32 v46, v0
	v_mov_b32_e32 v47, v0
	v_mov_b32_e32 v64, v0
	v_mov_b32_e32 v65, v0
	v_mov_b32_e32 v66, v0
	v_mov_b32_e32 v67, v0
	v_mov_b32_e32 v68, v0
	v_mov_b32_e32 v69, v0
	v_mov_b32_e32 v70, v0
	v_mov_b32_e32 v71, v0
	v_mov_b32_e32 v80, v0
	v_mov_b32_e32 v81, v0
	v_mov_b32_e32 v82, v0
	v_mov_b32_e32 v83, v0
	v_mov_b32_e32 v84, v0
	v_mov_b32_e32 v85, v0
	v_mov_b32_e32 v86, v0
	v_mov_b32_e32 v87, v0
	v_mov_b32_e32 v96, v0
	v_mov_b32_e32 v97, v0
	v_mov_b32_e32 v98, v0
	v_mov_b32_e32 v99, v0
	v_mov_b32_e32 v100, v0
	v_mov_b32_e32 v101, v0
	v_mov_b32_e32 v102, v0
	v_mov_b32_e32 v103, v0
	v_mov_b32_e32 v112, v0
	v_mov_b32_e32 v113, v0
	v_mov_b32_e32 v114, v0
	v_mov_b32_e32 v115, v0
	v_mov_b32_e32 v116, v0
	v_mov_b32_e32 v117, v0
	v_mov_b32_e32 v118, v0
	v_mov_b32_e32 v119, v0
	v_mov_b32_e32 v128, v0
	v_mov_b32_e32 v129, v0
	v_mov_b32_e32 v130, v0
	v_mov_b32_e32 v131, v0
	v_mov_b32_e32 v132, v0
	v_mov_b32_e32 v133, v0
	v_mov_b32_e32 v134, v0
	v_mov_b32_e32 v135, v0
	v_mov_b32_e32 v88, v0
	v_mov_b32_e32 v89, v0
	v_mov_b32_e32 v90, v0
	v_mov_b32_e32 v91, v0
	v_mov_b32_e32 v92, v0
	v_mov_b32_e32 v93, v0
	v_mov_b32_e32 v94, v0
	v_mov_b32_e32 v95, v0
	v_mov_b32_e32 v104, v0
	v_mov_b32_e32 v105, v0
	v_mov_b32_e32 v106, v0
	v_mov_b32_e32 v107, v0
	v_mov_b32_e32 v108, v0
	v_mov_b32_e32 v109, v0
	v_mov_b32_e32 v110, v0
	v_mov_b32_e32 v111, v0
	v_mov_b32_e32 v120, v0
	v_mov_b32_e32 v121, v0
	v_mov_b32_e32 v122, v0
	v_mov_b32_e32 v123, v0
	v_mov_b32_e32 v124, v0
	v_mov_b32_e32 v125, v0
	v_mov_b32_e32 v126, v0
	v_mov_b32_e32 v127, v0
	v_mov_b32_e32 v56, v0
	v_mov_b32_e32 v57, v0
	v_mov_b32_e32 v58, v0
	v_mov_b32_e32 v59, v0
	v_mov_b32_e32 v60, v0
	v_mov_b32_e32 v61, v0
	v_mov_b32_e32 v62, v0
	v_mov_b32_e32 v63, v0
	s_branch .LBB0_1731
	.p2alignl 6, 3212836864
